# lever 4: one static s_setprio 1 for waves 4-7 across the dense attention loop (reset to 0 at its exit)
# baseline (speedup 1.0000x reference)
; template<int THRL> __device__ __forceinline__ void attn_unit(int b,int qb,const unsigned char*Q,const unsigned char*__restrict__ K,const unsigned char*__restrict__ VT,unsigned char*O,char*shm){
;   const int tid=threadIdx.x,lane=tid&63,r32=lane&31,hi=lane>>5; const int wid=__builtin_amdgcn_readfirstlane(tid>>6);
;   const long rowbase=(long)b*SEQ; const int q0=qb*QB;
;   const unsigned char*Qw=Q+(rowbase+q0+wid*QBLK)*QP8;
;   const unsigned char*Kh=K+rowbase*KP8;
;   const unsigned lds0=(unsigned)(uintptr_t)shm;
;   float*wsf=(float*)(shm+LDS_WS)+wid*64;
;   const unsigned char*ksrc=Kh+(long)(32*(wid&1))*KP8+(wid>>1)*16; const unsigned klo=(unsigned)(lane&31)*KP8;
;   const unsigned char*vsrc=VT+(long)(32*(wid&1))*VTP+(wid>>1)*16; const unsigned vlo=(unsigned)(lane&31)*VTP;
;   const unsigned kdst=lds0+LDS_K+(wid>>1)*1024+(wid&1)*512, vdst=lds0+LDS_V+(wid>>1)*1024+(wid&1)*512;
;     ...
;   const char*Kbase=shm+LDS_K; bf16x8 kf[4];
;   const lds_cptr shm3=(lds_cptr)shm; const lds_cptr kp0=shm3+LDS_K+hi*2048+r32*16; const lds_cptr vp0=shm3+LDS_V+hi*2048+r32*16;
;   constexpr int NT=SEQ/KVBLK;
;   v8i_t q8; { const v4i_t qa=*reinterpret_cast<const v4i_t*>(Qw+(long)r32*QP8+32*hi), qb_=*reinterpret_cast<const v4i_t*>(Qw+(long)r32*QP8+32*hi+16); q8=__builtin_shufflevector(qa,qb_,0,1,2,3,4,5,6,7); }
;   const int one4_=((lane&15)==((lane>>4)&1))?0x38383838:0; const v8i_t vones={one4_,one4_,one4_,one4_,one4_,one4_,one4_,one4_};
;   const int nx=(grid%8==0)?8:1, x=block%nx, slot=block/nx, per=grid/nx;
;   for(int s8=x;s8<8;s8+=nx){ const int b=s8>>1,kvh=s8&1;
;     for(int u=slot;u<128;u+=per){ const int h=4*kvh+(u>>5),qb=u&31;
;       attn_unit<THRL>(b,qb,T.Q+h*D,T.K+kvh*D,T.VT+(long)(b*2+kvh)*D*SEQ,T.O+h*D,lds); } }
.LBB0_321:
	v_readlane_b32 s0, v254, 0
	v_readlane_b32 s1, v254, 1
	s_add_u32 s92, s0, 0x25400000
	s_addc_u32 s93, s1, 0
	s_add_u32 s0, s0, 0x20c00000
	s_addc_u32 s1, s1, 0
	v_readlane_b32 s2, v254, 12
	v_writelane_b32 v255, s0, 21
	v_readlane_b32 s3, v254, 13
	s_cmp_lt_i32 s2, 4
	v_writelane_b32 v255, s1, 22
	s_cselect_b64 s[0:1], -1, 0
	s_cmp_gt_i32 s3, 3
	s_cselect_b64 s[2:3], -1, 0
	s_and_b64 s[4:5], s[0:1], s[2:3]
	s_andn2_b64 vcc, exec, s[4:5]
	s_cbranch_vccnz .LBB0_423
	v_readlane_b32 s98, v254, 59
	s_nop 3
	s_cmp_ge_u32 s98, 4
	s_cbranch_scc0 .Lprio_d
	s_setprio 1
.Lprio_d:
	v_readlane_b32 s10, v254, 0
	v_readlane_b32 s11, v254, 1
	s_add_u32 s62, s10, 0x20c00200
	s_addc_u32 s63, s11, 0
	s_and_b64 s[0:1], s[12:13], exec
	s_cselect_b32 s64, 8, 1
	v_cvt_f32_ubyte0_e32 v1, s64
	v_rcp_iflag_f32_e32 v2, v1
	s_sub_i32 s2, 0, s64
	v_readlane_b32 s6, v254, 10
	s_abs_i32 s1, s6
	v_mul_f32_e32 v2, 0x4f7ffffe, v2
	v_cvt_u32_f32_e32 v2, v2
	v_writelane_b32 v255, s4, 17
	s_ashr_i32 s0, s6, 31
	v_and_b32_e32 v3, 63, v0
	v_readfirstlane_b32 s3, v2
	s_mul_i32 s2, s2, s3
	s_mul_hi_u32 s2, s3, s2
	s_add_i32 s3, s3, s2
	s_mul_hi_u32 s2, s1, s3
	v_writelane_b32 v255, s5, 18
	s_mul_i32 s4, s2, s64
	s_sub_i32 s1, s1, s4
	s_add_i32 s4, s2, 1
	s_sub_i32 s5, s1, s64
	s_cmp_ge_u32 s1, s64
	s_cselect_b32 s2, s4, s2
	s_cselect_b32 s1, s5, s1
	s_add_i32 s4, s2, 1
	s_cmp_ge_u32 s1, s64
	s_cselect_b32 s1, s4, s2
	s_xor_b32 s1, s1, s0
	s_sub_i32 s65, s1, s0
	v_readlane_b32 s1, v254, 9
	s_ashr_i32 s0, s1, 31
	s_abs_i32 s1, s1
	s_mul_hi_u32 s2, s1, s3
	s_mul_i32 s3, s2, s64
	s_sub_i32 s1, s1, s3
	s_add_i32 s3, s2, 1
	s_sub_i32 s4, s1, s64
	s_cmp_ge_u32 s1, s64
	s_cselect_b32 s2, s3, s2
	s_cselect_b32 s1, s4, s1
	s_add_i32 s3, s2, 1
	s_cmp_ge_u32 s1, s64
	s_cselect_b32 s1, s3, s2
	s_xor_b32 s1, s1, s0
	s_sub_i32 s66, s1, s0
	s_mul_i32 s0, s65, s64
	s_sub_i32 s8, s6, s0
	s_cmpk_lt_i32 s65, 0x80
	s_cselect_b64 s[0:1], -1, 0
	s_ashr_i32 s9, s8, 31
	s_add_i32 s4, 0, 0x10800
	s_lshl_b64 s[6:7], s[8:9], 19
	s_add_u32 s6, s10, s6
	s_addc_u32 s7, s11, s7
	s_add_u32 s67, s6, 0x19c00040
	v_and_b32_e32 v152, 31, v0
	v_bfe_u32 v4, v0, 5, 1
	s_addc_u32 s74, s7, 0
	s_lshl_b32 s75, s64, 19
	v_lshlrev_b32_e32 v2, 11, v4
	v_lshlrev_b32_e32 v5, 4, v152
	v_cmp_eq_u32_e64 s[2:3], 0, v3
	v_and_b32_e32 v3, 7, v0
	s_add_u32 s6, s10, 0x19402000
	v_add3_u32 v155, 0, v2, v5
	v_and_b32_e32 v5, 15, v0
	v_bfe_u32 v6, v0, 4, 1
	v_lshl_add_u32 v156, v3, 2, s4
	v_bfe_u32 v3, v0, 2, 4
	v_writelane_b32 v255, s6, 23
	s_addc_u32 s6, s11, 0
	v_mov_b32_e32 v7, 0x38383838
	v_cmp_eq_u32_e32 vcc, v5, v6
	v_lshlrev_b32_e32 v161, 6, v3
	v_lshlrev_b32_e32 v148, 10, v3
	v_or_b32_e32 v3, 16, v3
	s_bitcmp1_b32 s8, 0
	v_mov_b32_e32 v2, 0
	v_cndmask_b32_e32 v98, 0, v7, vcc
	v_lshlrev_b32_e32 v159, 4, v4
	v_lshlrev_b32_e32 v160, 8, v4
	v_lshlrev_b32_e32 v4, 4, v0
	v_lshlrev_b32_e32 v162, 6, v3
	v_lshlrev_b32_e32 v150, 10, v3
	s_cselect_b64 s[10:11], -1, 0
	s_bitcmp1_b32 s64, 0
	v_cndmask_b32_e64 v3, 0, 1, s[0:1]
	v_mov_b32_e32 v1, v0
	v_lshlrev_b32_e32 v153, 7, v152
	v_lshlrev_b32_e32 v154, 13, v152
	v_lshlrev_b32_e32 v142, 9, v152
	v_mov_b32_e32 v143, v2
	v_and_b32_e32 v144, 32, v0
	v_mov_b32_e32 v145, v2
	v_mov_b32_e32 v99, v98
	v_mov_b32_e32 v100, v98
	v_mov_b32_e32 v101, v98
	v_mov_b32_e32 v102, v98
	v_mov_b32_e32 v103, v98
	v_mov_b32_e32 v104, v98
	v_mov_b32_e32 v105, v98
	v_cmp_gt_u32_e64 s[4:5], 2, v5
	v_lshlrev_b32_e32 v157, 6, v5
	v_and_b32_e32 v158, 48, v0
	v_and_b32_e32 v146, 48, v4
	v_mov_b32_e32 v147, v2
	v_mov_b32_e32 v149, v2
	v_mov_b32_e32 v151, v2
	v_writelane_b32 v255, s6, 25
	s_cselect_b64 s[12:13], -1, 0
	v_mov_b32_e32 v163, 0x75757575
	v_mov_b32_e32 v164, 0x7f7f7f7f
	s_mov_b32 s82, 0x7050301
	v_cmp_ne_u32_e64 s[6:7], 1, v3
	s_branch .LBB0_324

; template<int THRL> __device__ __forceinline__ void attn_unit(int b,int qb,const unsigned char*Q,const unsigned char*__restrict__ K,const unsigned char*__restrict__ VT,unsigned char*O,char*shm){
;     ...
;       o[0]=pv8(p8B,vf[0],vf[1],o[0]); o[1]=pv8(p8B,vf[2],vf[3],o[1]); o2=__builtin_amdgcn_mfma_scale_f32_16x16x128_f8f6f4(p8B,vones,o2,1,0,0,0x7f7f7f7f,0,0x7f7f7f7f); }
;     ...
;   if((lane&15)<2){
;     #pragma unroll
;     for(int i=0;i<4;++i)wsf[32+16*(lane&15)+4*(lane>>4)+i]=o2[i]; }
.LBB0_341:
	s_and_b32 s0, s73, 0x3fffffc0
	s_lshl_b32 s0, s0, 2
	s_add_i32 s14, s0, 0
	s_and_saveexec_b64 s[22:23], s[4:5]
	s_cbranch_execz .LBB0_326
	v_mfma_scale_f32_16x16x128_f8f6f4 v[4:7], v[114:121], v[98:105], v[138:141], v164, v164 op_sel_hi:[0,0,0] cbsz:1
	v_add3_u32 v3, s14, v157, v158
	s_nop 10
	ds_write_b128 v3, v[4:7] offset:32896
	s_branch .LBB0_326
.Lprio_dx:
	s_setprio 0
